# ATT0 tile loop: in-wave MFMA/VALU interleave; both K/V LDS-DMA issue groups of each tile pair sunk into the QK MFMA shadows (end-of-iteration group guarded by a first-iteration flag)
# baseline (speedup 1.0000x reference)
.LBB0_502:
	v_mul_f32_e32 v0, v96, v0
	v_mul_f32_e32 v1, v96, v1
	v_mul_f32_e32 v21, v96, v21
	v_mul_f32_e32 v0, v0, v157
	v_mul_f32_e32 v1, v1, v156
	v_mul_f32_e32 v21, v21, v143
	v_med3_f32 v0, v0, s70, v178
	v_med3_f32 v1, v1, s70, v178
	v_mov_b32_e32 v143, v153
	v_cvt_pk_fp8_f32 v143, v0, v1
	v_mul_f32_e32 v2, v96, v2
	v_mul_f32_e32 v3, v96, v3
	v_mul_f32_e32 v2, v2, v155
	v_mul_f32_e32 v3, v3, v154
	v_mul_f32_e32 v20, v96, v20
	v_med3_f32 v0, v2, s70, v178
	v_med3_f32 v1, v3, s70, v178
	v_mul_f32_e32 v20, v20, v144
	v_mul_f32_e32 v10, v96, v10
	v_cvt_pk_fp8_f32 v143, v0, v1 op_sel:[0,0,1]
	v_med3_f32 v0, v94, s70, v178
	v_med3_f32 v1, v95, s70, v178
	v_mov_b32_e32 v144, v153
	v_mul_f32_e32 v10, v10, v145
	v_cvt_pk_fp8_f32 v144, v0, v1
	v_med3_f32 v0, v90, s70, v178
	v_med3_f32 v1, v91, s70, v178
	v_mov_b32_e32 v145, v153
	v_cvt_pk_fp8_f32 v145, v0, v1
	v_mul_f32_e32 v9, v96, v9
	v_med3_f32 v0, v88, s70, v178
	v_med3_f32 v1, v89, s70, v178
	v_mul_f32_e32 v8, v96, v8
	v_mul_f32_e32 v9, v9, v146
	v_cvt_pk_fp8_f32 v145, v0, v1 op_sel:[0,0,1]
	v_med3_f32 v0, v86, s70, v178
	v_med3_f32 v1, v87, s70, v178
	v_mov_b32_e32 v146, v153
	v_mul_f32_e32 v8, v8, v147
	v_cvt_pk_fp8_f32 v146, v0, v1
	v_med3_f32 v0, v82, s70, v178
	v_med3_f32 v1, v83, s70, v178
	v_mov_b32_e32 v147, v153
	v_cvt_pk_fp8_f32 v147, v0, v1
	v_mul_f32_e32 v5, v96, v5
	v_mul_f32_e32 v5, v5, v182
	v_med3_f32 v0, v80, s70, v178
	v_med3_f32 v1, v81, s70, v178
	v_lshlrev_b32_e32 v182, 4, v180
	v_cvt_pk_fp8_f32 v147, v0, v1 op_sel:[0,0,1]
	v_add_u32_e32 v0, s80, v182
	v_ashrrev_i32_e32 v1, 31, v0
	v_med3_f32 v2, v92, s70, v178
	v_med3_f32 v3, v93, s70, v178
	v_add_u32_sdwa v1, v0, v1 dst_sel:DWORD dst_unused:UNUSED_PAD src0_sel:DWORD src1_sel:BYTE_3
	v_cvt_pk_fp8_f32 v144, v2, v3 op_sel:[0,0,1]
	v_med3_f32 v2, v84, s70, v178
	v_med3_f32 v3, v85, s70, v178
	v_ashrrev_i32_e32 v1, 8, v1
	v_cvt_pk_fp8_f32 v146, v2, v3 op_sel:[0,0,1]
	v_mul_i32_i24_e32 v2, 0x100, v1
	v_sub_u32_e32 v2, v0, v2
	v_ashrrev_i32_e32 v2, 4, v2
	v_bitop3_b32 v2, v2, v1, 15 bitop3:0x78
	v_lshlrev_b32_e32 v3, 4, v2
	v_cmp_gt_i32_e32 vcc, 12, v2
	v_mul_f32_e32 v11, v96, v11
	v_mul_f32_e32 v11, v11, v152
	v_cndmask_b32_e32 v2, 0, v3, vcc
	v_mad_i32_i24 v152, v1, s88, v2
	v_add_u32_e32 v1, 0x2000, v0
	v_ashrrev_i32_e32 v2, 31, v1
	v_add_u32_sdwa v2, v1, v2 dst_sel:DWORD dst_unused:UNUSED_PAD src0_sel:DWORD src1_sel:BYTE_3
	s_mul_i32 s5, s6, 0x6c0000
	v_ashrrev_i32_e32 v2, 8, v2
	s_mul_hi_i32 s4, s6, 0x6c0000
	s_add_u32 s5, s68, s5
	v_mul_i32_i24_e32 v3, 0x100, v2
	s_addc_u32 s4, s69, s4
	v_mul_f32_e32 v4, v96, v4
	v_sub_u32_e32 v3, v1, v3
	s_add_u32 s64, s5, s7
	v_mul_f32_e32 v22, v96, v22
	v_mul_f32_e32 v4, v4, v184
	v_ashrrev_i32_e32 v3, 4, v3
	s_addc_u32 s65, s4, 0
	s_mul_i32 s5, s6, 0x1200000
	v_mul_f32_e32 v22, v22, v142
	v_med3_f32 v4, v4, s70, v178
	v_med3_f32 v5, v5, s70, v178
	v_mov_b32_e32 v142, v153
	v_bitop3_b32 v3, v3, v2, 15 bitop3:0x78
	s_mul_hi_i32 s4, s6, 0x1200000
	s_add_u32 s5, s12, s5
	v_cvt_pk_fp8_f32 v142, v4, v5
	v_lshlrev_b32_e32 v4, 4, v3
	v_cmp_gt_i32_e32 vcc, 12, v3
	s_addc_u32 s6, s13, s4
	s_lshl_b32 s4, s59, 9
	v_cndmask_b32_e32 v3, 0, v4, vcc
	s_add_u32 s4, s5, s4
	v_mul_f32_e32 v48, v48, v96
	v_mul_f32_e32 v49, v49, v96
	v_mad_i32_i24 v154, v2, s88, v3
	v_bfe_u32 v2, v180, 2, 2
	v_lshrrev_b32_e32 v4, 1, v180
	s_addc_u32 s5, s6, 0
	v_mul_f32_e32 v48, v48, v108
	v_mul_f32_e32 v49, v49, v107
	v_mul_f32_e32 v25, v96, v25
	v_and_b32_e32 v3, 48, v182
	v_and_or_b32 v2, v4, 8, v2
	v_ashrrev_i32_e32 v4, 8, v0
	v_lshrrev_b32_e32 v0, 3, v0
	s_movk_i32 s6, 0xc0
	v_mul_f32_e32 v25, v25, v131
	v_med3_f32 v48, v48, s70, v178
	v_med3_f32 v49, v49, s70, v178
	v_mov_b32_e32 v131, v153
	v_and_or_b32 v0, v0, s6, v3
	v_and_b32_e32 v3, 0x7fff0, v4
	v_lshrrev_b32_e32 v4, 1, v4
	s_add_u32 s66, s4, 0x58200100
	v_mul_f32_e32 v23, v96, v23
	v_cvt_pk_fp8_f32 v131, v48, v49
	v_and_b32_e32 v4, 4, v4
	s_addc_u32 s67, s5, 0
	v_mul_f32_e32 v50, v50, v96
	v_mul_f32_e32 v51, v51, v96
	v_mul_f32_e32 v23, v23, v141
	v_med3_f32 v8, v8, s70, v178
	v_med3_f32 v9, v9, s70, v178
	v_mov_b32_e32 v141, v153
	v_or3_b32 v3, v3, v4, v2
	v_ashrrev_i32_e32 v1, 8, v1
	s_add_i32 s56, s80, 0
	v_mul_f32_e32 v50, v50, v106
	v_mul_f32_e32 v51, v51, v105
	v_cvt_pk_fp8_f32 v141, v8, v9
	v_lshl_or_b32 v156, v3, 13, v0
	v_and_b32_e32 v3, 0x7fff0, v1
	v_lshrrev_b32_e32 v1, 1, v1
	s_add_i32 s57, s56, 0x8000
	s_add_i32 s86, s56, 0xa000
	v_ashrrev_i32_e32 v183, 5, v180
	v_med3_f32 v48, v50, s70, v178
	v_med3_f32 v49, v51, s70, v178
	v_and_b32_e32 v1, 4, v1
	s_mov_b32 m0, s57
	s_cmp_lg_u32 0, -1
	v_mul_f32_e32 v7, v96, v7
	v_cvt_pk_fp8_f32 v131, v48, v49 op_sel:[0,0,1]
	v_or3_b32 v1, v3, v1, v2
	global_load_lds_dwordx4 v152, s[64:65]
	s_mov_b32 m0, s86
	s_cselect_b32 s6, 0, 0
	s_add_i32 s91, s56, 0x2000
	v_lshlrev_b32_e32 v48, 1, v183
	v_mul_f32_e32 v7, v7, v158
	v_med3_f32 v8, v10, s70, v178
	v_med3_f32 v9, v11, s70, v178
	v_lshl_or_b32 v158, v1, 13, v0
	global_load_lds_dwordx4 v154, s[64:65]
	s_mov_b32 m0, s56
	s_add_u32 s38, s64, 0x30000
	v_bitop3_b32 v0, v48, v180, 15 bitop3:0x78
	v_cvt_pk_fp8_f32 v141, v8, v9 op_sel:[0,0,1]
	global_load_lds_dwordx4 v156, s[66:67]
	s_mov_b32 m0, s91
	s_addc_u32 s39, s65, 0
	s_add_i32 s95, s56, 0xc000
	v_lshlrev_b32_e32 v49, 8, v181
	v_lshlrev_b32_e32 v8, 4, v0
	v_mul_f32_e32 v6, v96, v6
	global_load_lds_dwordx4 v158, s[66:67]
	s_mov_b32 m0, s95
	s_add_i32 s18, s56, 0xe000
	v_add_u32_e32 v4, v8, v49
	v_mul_f32_e32 v60, v60, v96
	v_mul_f32_e32 v61, v61, v96
	v_mul_f32_e32 v56, v56, v96
	v_mul_f32_e32 v57, v57, v96
	v_mul_f32_e32 v52, v52, v96
	v_mul_f32_e32 v53, v53, v96
	v_mul_f32_e32 v44, v96, v44
	v_mul_f32_e32 v45, v96, v45
	v_mul_f32_e32 v40, v96, v40
	v_mul_f32_e32 v41, v96, v41
	v_mul_f32_e32 v36, v96, v36
	v_mul_f32_e32 v37, v96, v37
	v_mul_f32_e32 v32, v96, v32
	v_mul_f32_e32 v33, v96, v33
	v_mul_f32_e32 v6, v6, v159
	global_load_lds_dwordx4 v152, s[38:39]
	s_mov_b32 m0, s18
	v_add_u32_e32 v184, 0, v4
	v_xor_b32_e32 v4, 16, v4
	v_mul_f32_e32 v60, v60, v104
	v_mul_f32_e32 v61, v61, v103
	v_mul_f32_e32 v56, v56, v100
	v_mul_f32_e32 v57, v57, v99
	v_mul_f32_e32 v52, v52, v112
	v_mul_f32_e32 v53, v53, v111
	v_mul_f32_e32 v44, v44, v120
	v_mul_f32_e32 v45, v45, v119
	v_mul_f32_e32 v40, v40, v116
	v_mul_f32_e32 v41, v41, v115
	v_mul_f32_e32 v36, v36, v128
	v_mul_f32_e32 v37, v37, v127
	v_mul_f32_e32 v32, v32, v124
	v_mul_f32_e32 v33, v33, v123
	v_mul_f32_e32 v29, v96, v29
	v_mul_f32_e32 v30, v96, v30
	v_mul_f32_e32 v31, v96, v31
	v_mul_f32_e32 v24, v96, v24
	v_mul_f32_e32 v26, v96, v26
	v_mul_f32_e32 v27, v96, v27
	v_med3_f32 v6, v6, s70, v178
	v_med3_f32 v7, v7, s70, v178
	global_load_lds_dwordx4 v154, s[38:39]
	v_add_u32_e32 v185, 0, v4
	v_mul_f32_e32 v29, v29, v135
	v_mul_f32_e32 v30, v30, v134
	v_mul_f32_e32 v31, v31, v133
	v_mul_f32_e32 v24, v24, v132
	v_mul_f32_e32 v26, v26, v130
	v_mul_f32_e32 v27, v27, v129
	v_med3_f32 v60, v60, s70, v178
	v_med3_f32 v61, v61, s70, v178
	v_mov_b32_e32 v128, v153
	v_med3_f32 v56, v56, s70, v178
	v_med3_f32 v57, v57, s70, v178
	v_mov_b32_e32 v129, v153
	v_med3_f32 v52, v52, s70, v178
	v_med3_f32 v53, v53, s70, v178
	v_mov_b32_e32 v130, v153
	v_med3_f32 v44, v44, s70, v178
	v_med3_f32 v45, v45, s70, v178
	v_mov_b32_e32 v132, v153
	v_med3_f32 v40, v40, s70, v178
	v_med3_f32 v41, v41, s70, v178
	v_mov_b32_e32 v133, v153
	v_med3_f32 v36, v36, s70, v178
	v_med3_f32 v37, v37, s70, v178
	v_mov_b32_e32 v134, v153
	v_med3_f32 v32, v32, s70, v178
	v_med3_f32 v33, v33, s70, v178
	v_mov_b32_e32 v135, v153
	v_cvt_pk_fp8_f32 v142, v6, v7 op_sel:[0,0,1]
	s_waitcnt vmcnt(0)
	s_waitcnt vmcnt(0) lgkmcnt(0)
	s_barrier
	ds_read_b128 v[0:3], v184 offset:32768
	ds_read_b128 v[4:7], v185 offset:32768
	v_mul_f32_e32 v12, v96, v12
	v_mul_f32_e32 v13, v96, v13
	v_cvt_pk_fp8_f32 v128, v60, v61
	v_cvt_pk_fp8_f32 v129, v56, v57
	v_cvt_pk_fp8_f32 v130, v52, v53
	v_cvt_pk_fp8_f32 v132, v44, v45
	v_cvt_pk_fp8_f32 v133, v40, v41
	v_cvt_pk_fp8_f32 v134, v36, v37
	v_cvt_pk_fp8_f32 v135, v32, v33
	v_mul_f32_e32 v62, v62, v96
	v_mul_f32_e32 v63, v63, v96
	v_mul_f32_e32 v58, v58, v96
	v_mul_f32_e32 v59, v59, v96
	v_mul_f32_e32 v54, v54, v96
	v_mul_f32_e32 v55, v55, v96
	v_mul_f32_e32 v46, v96, v46
	v_mul_f32_e32 v47, v96, v47
	v_mul_f32_e32 v42, v96, v42
	v_mul_f32_e32 v43, v96, v43
	v_mul_f32_e32 v38, v96, v38
	v_mul_f32_e32 v39, v96, v39
	v_mul_f32_e32 v34, v96, v34
	v_mul_f32_e32 v35, v96, v35
	v_mul_f32_e32 v16, v96, v16
	v_mul_f32_e32 v12, v12, v151
	v_mul_f32_e32 v13, v13, v150
	v_mul_f32_e32 v62, v62, v102
	v_mul_f32_e32 v63, v63, v101
	v_mul_f32_e32 v58, v58, v98
	v_mul_f32_e32 v59, v59, v97
	v_mul_f32_e32 v54, v54, v110
	v_mul_f32_e32 v55, v55, v109
	v_mul_f32_e32 v46, v46, v118
	v_mul_f32_e32 v47, v47, v117
	v_mul_f32_e32 v42, v42, v114
	v_mul_f32_e32 v43, v43, v113
	v_mul_f32_e32 v38, v38, v126
	v_mul_f32_e32 v39, v39, v125
	v_mul_f32_e32 v34, v34, v122
	v_mul_f32_e32 v35, v35, v121
	v_mul_f32_e32 v16, v16, v140
	v_med3_f32 v12, v12, s70, v178
	v_med3_f32 v13, v13, s70, v178
	v_mov_b32_e32 v140, v153
	v_med3_f32 v62, v62, s70, v178
	v_med3_f32 v63, v63, s70, v178
	v_med3_f32 v56, v58, s70, v178
	v_med3_f32 v57, v59, s70, v178
	v_med3_f32 v54, v54, s70, v178
	v_med3_f32 v55, v55, s70, v178
	v_med3_f32 v46, v46, s70, v178
	v_med3_f32 v47, v47, s70, v178
	v_med3_f32 v40, v42, s70, v178
	v_med3_f32 v41, v43, s70, v178
	v_med3_f32 v38, v38, s70, v178
	v_med3_f32 v39, v39, s70, v178
	v_med3_f32 v32, v34, s70, v178
	v_med3_f32 v33, v35, s70, v178
	v_cvt_pk_fp8_f32 v140, v12, v13
	v_or_b32_e32 v50, 0x2000, v49
	v_mul_f32_e32 v17, v96, v17
	v_mul_f32_e32 v14, v96, v14
	v_mul_f32_e32 v15, v96, v15
	v_cvt_pk_fp8_f32 v128, v62, v63 op_sel:[0,0,1]
	v_cvt_pk_fp8_f32 v129, v56, v57 op_sel:[0,0,1]
	v_cvt_pk_fp8_f32 v130, v54, v55 op_sel:[0,0,1]
	v_cvt_pk_fp8_f32 v132, v46, v47 op_sel:[0,0,1]
	v_cvt_pk_fp8_f32 v133, v40, v41 op_sel:[0,0,1]
	v_cvt_pk_fp8_f32 v134, v38, v39 op_sel:[0,0,1]
	v_cvt_pk_fp8_f32 v135, v32, v33 op_sel:[0,0,1]
	v_add_u32_e32 v12, v8, v50
	v_mul_f32_e32 v17, v17, v139
	v_mul_f32_e32 v14, v14, v149
	v_mul_f32_e32 v15, v15, v148
	v_xor_b32_e32 v12, 16, v12
	v_med3_f32 v16, v16, s70, v178
	v_med3_f32 v17, v17, s70, v178
	v_mov_b32_e32 v139, v153
	v_med3_f32 v14, v14, s70, v178
	v_med3_f32 v15, v15, s70, v178
	v_add_u32_e32 v186, 0, v12
	v_cvt_pk_fp8_f32 v139, v16, v17
	v_cvt_pk_fp8_f32 v140, v14, v15 op_sel:[0,0,1]
	ds_read_b128 v[8:11], v184 offset:40960
	ds_read_b128 v[12:15], v186 offset:32768
	v_mul_f32_e32 v18, v96, v18
	v_mul_f32_e32 v19, v96, v19
	s_waitcnt lgkmcnt(2)
	v_mfma_f32_32x32x64_f8f6f4 v[32:47], v[0:7], v[128:135], 0
	v_med3_f32 v0, v74, s70, v178
	v_med3_f32 v1, v75, s70, v178
	v_mov_b32_e32 v149, v153
	v_mul_f32_e32 v28, v96, v28
	v_mul_f32_e32 v18, v18, v138
	v_mul_f32_e32 v19, v19, v137
	v_cvt_pk_fp8_f32 v149, v0, v1
	v_mul_f32_e32 v28, v28, v136
	v_med3_f32 v16, v18, s70, v178
	v_med3_f32 v17, v19, s70, v178
	v_med3_f32 v28, v28, s70, v178
	v_med3_f32 v29, v29, s70, v178
	v_mov_b32_e32 v136, v153
	v_med3_f32 v24, v24, s70, v178
	v_med3_f32 v25, v25, s70, v178
	v_mov_b32_e32 v137, v153
	v_med3_f32 v20, v20, s70, v178
	v_med3_f32 v21, v21, s70, v178
	v_mov_b32_e32 v138, v153
	v_cvt_pk_fp8_f32 v139, v16, v17 op_sel:[0,0,1]
	v_med3_f32 v16, v78, s70, v178
	v_med3_f32 v17, v79, s70, v178
	v_mov_b32_e32 v148, v153
	v_cvt_pk_fp8_f32 v136, v28, v29
	v_cvt_pk_fp8_f32 v137, v24, v25
	v_cvt_pk_fp8_f32 v138, v20, v21
	v_cvt_pk_fp8_f32 v148, v16, v17
	v_med3_f32 v0, v70, s70, v178
	v_med3_f32 v1, v71, s70, v178
	v_cvt_pk_fp8_f32 v149, v0, v1 op_sel:[0,0,1]
	v_med3_f32 v0, v68, s70, v178
	v_med3_f32 v1, v69, s70, v178
	v_mov_b32_e32 v150, v153
	v_cvt_pk_fp8_f32 v150, v0, v1
	v_add_u32_e32 v0, 4, v48
	v_med3_f32 v30, v30, s70, v178
	v_med3_f32 v31, v31, s70, v178
	v_med3_f32 v24, v26, s70, v178
	v_med3_f32 v25, v27, s70, v178
	v_med3_f32 v22, v22, s70, v178
	v_med3_f32 v23, v23, s70, v178
	v_med3_f32 v18, v76, s70, v178
	v_med3_f32 v19, v77, s70, v178
	v_bitop3_b32 v0, v0, v180, 15 bitop3:0x78
	v_cvt_pk_fp8_f32 v136, v30, v31 op_sel:[0,0,1]
	v_cvt_pk_fp8_f32 v137, v24, v25 op_sel:[0,0,1]
	v_cvt_pk_fp8_f32 v138, v22, v23 op_sel:[0,0,1]
	v_cvt_pk_fp8_f32 v148, v18, v19 op_sel:[0,0,1]
	s_waitcnt lgkmcnt(0)
	v_mfma_f32_32x32x64_f8f6f4 v[16:31], v[8:15], v[128:135], 0
	v_lshlrev_b32_e32 v8, 4, v0
	v_add_u32_e32 v4, v8, v49
	v_add_u32_e32 v187, 0, v4
	v_xor_b32_e32 v4, 16, v4
	v_add_u32_e32 v188, 0, v4
	ds_read_b128 v[0:3], v187 offset:32768
	ds_read_b128 v[4:7], v188 offset:32768
	v_add_u32_e32 v12, v8, v50
	v_xor_b32_e32 v12, 16, v12
	v_add_u32_e32 v189, 0, v12
	v_med3_f32 v53, v66, s70, v178
	v_med3_f32 v54, v67, s70, v178
	v_mov_b32_e32 v151, v153
	ds_read_b128 v[8:11], v187 offset:40960
	ds_read_b128 v[12:15], v189 offset:32768
	v_cvt_pk_fp8_f32 v151, v53, v54
	s_waitcnt lgkmcnt(2)
	v_mfma_f32_32x32x64_f8f6f4 v[32:47], v[0:7], v[136:143], v[32:47]
	v_med3_f32 v0, v64, s70, v178
	v_med3_f32 v1, v65, s70, v178
	v_cvt_pk_fp8_f32 v151, v0, v1 op_sel:[0,0,1]
	v_lshlrev_b32_e32 v0, 3, v180
	v_and_b32_e32 v1, 0xc0, v182
	v_lshlrev_b32_e32 v2, 1, v180
	v_and_or_b32 v1, v0, 24, v1
	v_and_b32_e32 v2, 32, v2
	v_and_b32_e32 v0, 0x100, v0
	v_or3_b32 v56, v1, v2, v0
	v_add_u32_e32 v0, 8, v48
	v_bitop3_b32 v0, v0, v180, 15 bitop3:0x78
	v_med3_f32 v51, v72, s70, v178
	v_med3_f32 v52, v73, s70, v178
	v_cvt_pk_fp8_f32 v150, v51, v52 op_sel:[0,0,1]
	s_waitcnt lgkmcnt(0)
	v_mfma_f32_32x32x64_f8f6f4 v[16:31], v[8:15], v[136:143], v[16:31]
	v_lshlrev_b32_e32 v8, 4, v0
	v_add_u32_e32 v4, v8, v49
	v_add_u32_e32 v191, 0, v4
	v_xor_b32_e32 v4, 16, v4
	v_add_u32_e32 v192, 0, v4
	ds_read_b128 v[0:3], v191 offset:32768
	ds_read_b128 v[4:7], v192 offset:32768
	v_add_u32_e32 v8, v8, v50
	v_xor_b32_e32 v8, 16, v8
	s_mov_b32 s36, s37
	v_add_u32_e32 v193, 0, v8
	ds_read_b128 v[48:51], v191 offset:40960
	ds_read_b128 v[52:55], v193 offset:32768
	s_mov_b32 s38, s37
	s_mov_b32 s39, s37
	s_waitcnt lgkmcnt(2)
	v_mfma_f32_32x32x64_f8f6f4 v[32:47], v[0:7], v[144:151], v[32:47]
	s_mov_b32 s40, s37
	s_mov_b32 s41, s37
	s_mov_b32 s42, s37
	s_mov_b32 s43, s37
	s_mov_b32 s44, s37
	s_mov_b32 s45, s37
	s_mov_b32 s46, s37
	s_mov_b32 s47, s37
	s_mov_b32 s48, s37
	s_mov_b32 s49, s37
	s_mov_b32 s50, s37
	s_mov_b32 s51, s37
	v_mov_b64_e32 v[0:1], s[36:37]
	v_mov_b64_e32 v[2:3], s[38:39]
	v_mov_b64_e32 v[4:5], s[40:41]
	v_mov_b64_e32 v[6:7], s[42:43]
	v_mov_b64_e32 v[8:9], s[44:45]
	v_mov_b64_e32 v[10:11], s[46:47]
	v_mov_b64_e32 v[12:13], s[48:49]
	v_mov_b64_e32 v[14:15], s[50:51]
	s_add_u32 s38, s64, 0x60000
	s_addc_u32 s39, s65, 0
	s_mov_b32 m0, s57
	s_add_u32 s4, s4, 0x58280100
	s_waitcnt lgkmcnt(0)
	s_waitcnt lgkmcnt(0)
	s_barrier
	global_load_lds_dwordx4 v152, s[38:39]
	s_mov_b32 m0, s86
	s_addc_u32 s5, s5, 0
	s_add_i32 s40, s56, 0x4000
	global_load_lds_dwordx4 v154, s[38:39]
	s_mov_b32 m0, s40
	s_add_i32 s41, s56, 0x6000
	global_load_lds_dwordx4 v156, s[4:5]
	s_mov_b32 m0, s41
	v_mfma_f32_32x32x64_f8f6f4 v[16:31], v[48:55], v[144:151], v[16:31]
	global_load_lds_dwordx4 v158, s[4:5]
	v_max_f32_e32 v48, v33, v33
	v_max_f32_e32 v49, v32, v32
	v_max_f32_e32 v48, v49, v48
	v_max3_f32 v48, v48, v34, v35
	v_max3_f32 v48, v48, v36, v37
	v_max3_f32 v48, v48, v38, v39
	v_max3_f32 v48, v48, v40, v41
	v_max3_f32 v48, v48, v42, v43
	v_max3_f32 v48, v48, v44, v45
	v_max3_f32 v48, v48, v46, v47
	s_add_i32 s42, s33, -1
	v_add_u32_e32 v190, s6, v56
	s_mov_b32 s19, 4
	s_nop 5
	v_max3_f32 v48, v48, v16, v17
	v_max3_f32 v48, v48, v18, v19
	v_max3_f32 v48, v48, v20, v21
	v_max3_f32 v48, v48, v22, v23
	v_max3_f32 v48, v48, v24, v25
	v_max3_f32 v48, v48, v26, v27
	v_max3_f32 v48, v48, v28, v29
	v_max3_f32 v48, v48, v30, v31
	v_mov_b32_e32 v49, v48
	s_nop 1
	v_permlane32_swap_b32_e32 v48, v49
	v_max_f32_e32 v49, v49, v49
	v_max_f32_e32 v48, v48, v48
	v_max_f32_e32 v48, v48, v49
	v_add_f32_e32 v49, 0x7149f2ca, v48
	v_cmp_ge_f32_e32 vcc, s93, v49
	s_cmp_eq_u64 vcc, exec
	v_max_f32_e32 v49, 0xf149f2ca, v48
	s_cselect_b64 vcc, -1, 0
	v_cndmask_b32_e32 v195, v49, v179, vcc
	v_mul_f32_e32 v48, 0xbdd53b94, v195
	v_fmamk_f32 v32, v32, 0x3dd53b94, v48
	v_exp_f32_e32 v64, v32
	v_fmamk_f32 v32, v33, 0x3dd53b94, v48
	v_exp_f32_e32 v65, v32
	v_fmamk_f32 v32, v34, 0x3dd53b94, v48
	v_exp_f32_e32 v66, v32
	v_fmamk_f32 v32, v35, 0x3dd53b94, v48
	v_exp_f32_e32 v67, v32
	v_fmamk_f32 v32, v36, 0x3dd53b94, v48
	v_exp_f32_e32 v68, v32
	v_fmamk_f32 v32, v37, 0x3dd53b94, v48
	v_exp_f32_e32 v69, v32
	v_fmamk_f32 v32, v38, 0x3dd53b94, v48
	v_exp_f32_e32 v70, v32
	v_fmamk_f32 v32, v39, 0x3dd53b94, v48
	v_exp_f32_e32 v71, v32
	v_fmamk_f32 v32, v40, 0x3dd53b94, v48
	v_exp_f32_e32 v72, v32
	v_fmamk_f32 v32, v41, 0x3dd53b94, v48
	v_exp_f32_e32 v73, v32
	v_fmamk_f32 v32, v42, 0x3dd53b94, v48
	v_exp_f32_e32 v74, v32
	v_fmamk_f32 v32, v43, 0x3dd53b94, v48
	v_exp_f32_e32 v75, v32
	v_fmamk_f32 v32, v44, 0x3dd53b94, v48
	v_pk_fma_f32 v[86:87], v[22:23], s[54:55], v[48:49] op_sel_hi:[1,0,0]
	v_sub_f32_e32 v22, 0xf149f2ca, v49
	v_exp_f32_e32 v76, v32
	v_fmamk_f32 v32, v45, 0x3dd53b94, v48
	v_mul_f32_e32 v22, 0x3dd53b94, v22
	v_exp_f32_e32 v77, v32
	v_fmamk_f32 v32, v46, 0x3dd53b94, v48
	v_exp_f32_e32 v22, v22
	v_exp_f32_e32 v78, v32
	v_fmamk_f32 v32, v47, 0x3dd53b94, v48
	v_exp_f32_e32 v79, v32
	s_addk_i32 s6, 0x4000
	v_pk_fma_f32 v[94:95], v[30:31], s[54:55], v[48:49] op_sel_hi:[1,0,0]
	v_pk_fma_f32 v[92:93], v[28:29], s[54:55], v[48:49] op_sel_hi:[1,0,0]
	v_pk_fma_f32 v[90:91], v[26:27], s[54:55], v[48:49] op_sel_hi:[1,0,0]
	v_pk_fma_f32 v[88:89], v[24:25], s[54:55], v[48:49] op_sel_hi:[1,0,0]
	v_pk_fma_f32 v[84:85], v[20:21], s[54:55], v[48:49] op_sel_hi:[1,0,0]
	v_pk_fma_f32 v[82:83], v[18:19], s[54:55], v[48:49] op_sel_hi:[1,0,0]
	v_pk_fma_f32 v[80:81], v[16:17], s[54:55], v[48:49] op_sel_hi:[1,0,0]
	v_cndmask_b32_e64 v201, v22, 1.0, vcc
	v_add_u32_e32 v199, s6, v56
	v_mov_b64_e32 v[62:63], v[14:15]
	v_mov_b64_e32 v[46:47], v[14:15]
	v_mov_b64_e32 v[30:31], v[14:15]
	v_mov_b32_e32 v155, v153
	v_mov_b32_e32 v157, v153
	v_mov_b32_e32 v159, v153
	v_cmp_gt_u32_e64 s[4:5], 32, v180
	v_lshl_add_u32 v197, v181, 2, s77
	v_lshlrev_b32_e32 v196, 4, v183
	v_mov_b32_e32 v198, 0
	v_mov_b64_e32 v[60:61], v[12:13]
	v_mov_b64_e32 v[58:59], v[10:11]
	v_mov_b64_e32 v[56:57], v[8:9]
	v_mov_b64_e32 v[54:55], v[6:7]
	v_mov_b64_e32 v[52:53], v[4:5]
	v_mov_b64_e32 v[50:51], v[2:3]
	v_mov_b64_e32 v[48:49], v[0:1]
	v_mov_b64_e32 v[44:45], v[12:13]
	v_mov_b64_e32 v[42:43], v[10:11]
	v_mov_b64_e32 v[40:41], v[8:9]
	v_mov_b64_e32 v[38:39], v[6:7]
	v_mov_b64_e32 v[36:37], v[4:5]
	v_mov_b64_e32 v[34:35], v[2:3]
	v_mov_b64_e32 v[32:33], v[0:1]
	v_mov_b64_e32 v[28:29], v[12:13]
	v_mov_b64_e32 v[26:27], v[10:11]
	v_mov_b64_e32 v[24:25], v[8:9]
	v_mov_b64_e32 v[22:23], v[6:7]
	v_mov_b64_e32 v[20:21], v[4:5]
	v_mov_b64_e32 v[18:19], v[2:3]
	v_mov_b64_e32 v[16:17], v[0:1]
	s_mov_b32 vcc_lo, 0
.LBB0_503:
	s_add_i32 s36, s19, -3
	s_cmp_lt_u32 s36, s33
	s_cselect_b64 s[6:7], -1, 0
	s_cmp_ge_u32 s36, s33
	ds_read_b128 v[100:103], v185 offset:49152
	ds_read_b128 v[96:99], v184 offset:49152
	ds_read_b128 v[104:107], v184 offset:57344
	ds_read_b128 v[108:111], v186 offset:49152
	ds_read_b128 v[224:227], v188 offset:49152
	ds_read_b128 v[220:223], v187 offset:49152
	ds_read_b128 v[228:231], v187 offset:57344
	ds_read_b128 v[232:235], v189 offset:49152
	v_add_f32_e32 v202, 0, v64
	v_add_f32_e32 v202, v65, v202
	v_add_f32_e32 v202, v66, v202
	v_add_f32_e32 v202, v67, v202
	v_add_f32_e32 v202, v68, v202
	v_add_f32_e32 v202, v69, v202
	v_add_f32_e32 v202, v70, v202
	v_add_f32_e32 v202, v71, v202
	v_add_f32_e32 v202, v72, v202
	v_add_f32_e32 v202, v73, v202
	s_waitcnt lgkmcnt(0)
	v_mfma_f32_32x32x64_f8f6f4 v[112:127], v[96:103], v[128:135], 0
	s_cmp_eq_u32 vcc_lo, 0
	s_cbranch_scc1 .Latt0_sk0
	v_lshl_add_u64 v[246:247], s[48:49], 0, v[152:153]
	s_mov_b32 m0, s57
	s_nop 0
	global_load_lds_dwordx4 v[246:247], off
.Latt0_sk0:
	v_add_f32_e32 v202, v74, v202
	v_add_f32_e32 v202, v75, v202
	v_exp_f32_e32 v80, v80
	v_add_f32_e32 v202, v76, v202
	v_exp_f32_e32 v81, v81
	v_add_f32_e32 v202, v77, v202
	v_exp_f32_e32 v82, v82
	v_add_f32_e32 v202, v78, v202
	v_mfma_f32_32x32x64_f8f6f4 v[96:111], v[104:111], v[128:135], 0
	s_cmp_eq_u32 vcc_lo, 0
	s_cbranch_scc1 .Latt0_sk1
	v_lshl_add_u64 v[246:247], s[48:49], 0, v[154:155]
	s_mov_b32 m0, s86
	s_nop 0
	global_load_lds_dwordx4 v[246:247], off
.Latt0_sk1:
	v_exp_f32_e32 v83, v83
	v_add_f32_e32 v202, v79, v202
	v_exp_f32_e32 v84, v84
	v_add_f32_e32 v202, v80, v202
	v_exp_f32_e32 v85, v85
	v_add_f32_e32 v202, v81, v202
	v_exp_f32_e32 v86, v86
	v_add_f32_e32 v202, v82, v202
	v_mfma_f32_32x32x64_f8f6f4 v[112:127], v[220:227], v[136:143], v[112:127]
	s_cmp_eq_u32 vcc_lo, 0
	s_cbranch_scc1 .Latt0_sk2
	v_lshl_add_u64 v[246:247], s[50:51], 0, v[156:157]
	s_mov_b32 m0, s40
	s_nop 0
	global_load_lds_dwordx4 v[246:247], off
.Latt0_sk2:
	v_exp_f32_e32 v87, v87
	v_add_f32_e32 v202, v83, v202
	v_exp_f32_e32 v88, v88
	v_add_f32_e32 v202, v84, v202
	v_exp_f32_e32 v89, v89
	v_add_f32_e32 v202, v85, v202
	v_exp_f32_e32 v90, v90
	v_add_f32_e32 v202, v86, v202
	v_mfma_f32_32x32x64_f8f6f4 v[96:111], v[228:235], v[136:143], v[96:111]
	s_cmp_eq_u32 vcc_lo, 0
	s_cbranch_scc1 .Latt0_sk3
	v_lshl_add_u64 v[246:247], s[50:51], 0, v[158:159]
	s_mov_b32 m0, s41
	s_nop 0
	global_load_lds_dwordx4 v[246:247], off
.Latt0_sk3:
	v_exp_f32_e32 v91, v91
	v_add_f32_e32 v202, v87, v202
	v_exp_f32_e32 v92, v92
	v_add_f32_e32 v202, v88, v202
	v_exp_f32_e32 v93, v93
	v_add_f32_e32 v202, v89, v202
	v_exp_f32_e32 v94, v94
	v_add_f32_e32 v202, v90, v202
	ds_read_b128 v[224:227], v192 offset:49152
	ds_read_b128 v[220:223], v191 offset:49152
	ds_read_b128 v[228:231], v191 offset:57344
	ds_read_b128 v[232:235], v193 offset:49152
	v_exp_f32_e32 v95, v95
	v_add_f32_e32 v202, v91, v202
	v_add_f32_e32 v202, v92, v202
	v_add_f32_e32 v202, v93, v202
	v_add_f32_e32 v202, v94, v202
	v_add_f32_e32 v202, v95, v202
	v_mov_b32_e32 v203, v202
	s_nop 1
	s_waitcnt lgkmcnt(0)
	v_mfma_f32_32x32x64_f8f6f4 v[112:127], v[220:227], v[144:151], v[112:127]
	v_permlane32_swap_b32_e32 v202, v203
	v_cvt_pk_bf16_f32 v204, v64, v65
	v_cvt_pk_bf16_f32 v205, v66, v67
	v_cvt_pk_bf16_f32 v206, v68, v69
	v_cvt_pk_bf16_f32 v207, v70, v71
	v_cvt_pk_bf16_f32 v208, v72, v73
	v_cvt_pk_bf16_f32 v209, v74, v75
	v_cvt_pk_bf16_f32 v210, v76, v77
	v_cvt_pk_bf16_f32 v211, v78, v79
	v_cvt_pk_bf16_f32 v212, v80, v81
	v_cvt_pk_bf16_f32 v213, v82, v83
	v_mfma_f32_32x32x64_f8f6f4 v[96:111], v[228:235], v[144:151], v[96:111]
	v_cvt_pk_bf16_f32 v214, v84, v85
	v_cvt_pk_bf16_f32 v215, v86, v87
	v_cvt_pk_bf16_f32 v216, v88, v89
	v_cvt_pk_bf16_f32 v217, v90, v91
	v_cvt_pk_bf16_f32 v218, v92, v93
	v_cvt_pk_bf16_f32 v219, v94, v95
	s_nop 0
	v_permlane32_swap_b32_e32 v204, v206
	v_permlane32_swap_b32_e32 v205, v207
	v_permlane32_swap_b32_e32 v208, v210
	v_permlane32_swap_b32_e32 v209, v211
	v_permlane32_swap_b32_e32 v212, v214
	v_permlane32_swap_b32_e32 v213, v215
	v_permlane32_swap_b32_e32 v216, v218
	v_permlane32_swap_b32_e32 v217, v219
	ds_read_b64_tr_b16 v[220:221], v190 offset:0
	ds_read_b64_tr_b16 v[222:223], v190 offset:0x800
	ds_read_b64_tr_b16 v[224:225], v190 offset:0x1000
	ds_read_b64_tr_b16 v[226:227], v190 offset:0x1800
	ds_read_b64_tr_b16 v[228:229], v190 offset:0x2000
	ds_read_b64_tr_b16 v[230:231], v190 offset:0x2800
	ds_read_b64_tr_b16 v[232:233], v190 offset:0x3000
	ds_read_b64_tr_b16 v[234:235], v190 offset:0x3800
	v_max_f32_e32 v200, v113, v113
	v_max_f32_e32 v240, v112, v112
	v_max_f32_e32 v200, v240, v200
	v_max3_f32 v200, v200, v114, v115
	v_max3_f32 v200, v200, v116, v117
	v_max3_f32 v200, v200, v118, v119
	v_max3_f32 v200, v200, v120, v121
	v_max3_f32 v200, v200, v122, v123
	s_waitcnt lgkmcnt(0)
	s_nop 0
	v_mfma_f32_32x32x16_bf16 v[0:15], v[204:207], v[220:223], v[0:15]
	v_max3_f32 v200, v200, v124, v125
	v_max3_f32 v200, v200, v126, v127
	v_max3_f32 v200, v200, v96, v97
	v_max3_f32 v200, v200, v98, v99
	v_max3_f32 v200, v200, v100, v101
	ds_read_b64_tr_b16 v[220:221], v190 offset:0x200
	ds_read_b64_tr_b16 v[222:223], v190 offset:0xa00
	v_mfma_f32_32x32x16_bf16 v[0:15], v[208:211], v[224:227], v[0:15]
	v_max3_f32 v200, v200, v102, v103
	v_max3_f32 v200, v200, v104, v105
	v_max3_f32 v200, v200, v106, v107
	v_max3_f32 v200, v200, v108, v109
	v_max3_f32 v200, v200, v110, v111
	ds_read_b64_tr_b16 v[224:225], v190 offset:0x1200
	ds_read_b64_tr_b16 v[226:227], v190 offset:0x1a00
	v_mfma_f32_32x32x16_bf16 v[0:15], v[212:215], v[228:231], v[0:15]
	v_mov_b32_e32 v240, v200
	s_nop 1
	v_permlane32_swap_b32_e32 v200, v240
	ds_read_b64_tr_b16 v[228:229], v190 offset:0x2200
	ds_read_b64_tr_b16 v[230:231], v190 offset:0x2a00
	ds_read_b64_tr_b16 v[236:237], v190 offset:0x3200
	ds_read_b64_tr_b16 v[238:239], v190 offset:0x3a00
	v_max_f32_e32 v240, v240, v240
	v_max_f32_e32 v200, v200, v200
	v_max_f32_e32 v200, v200, v240
	v_sub_f32_e32 v240, v200, v195
	v_cmp_ge_f32_e32 vcc, s93, v240
	v_max_f32_e32 v240, v195, v195
	v_max_f32_e32 v240, v240, v200
	v_sub_f32_e32 v200, v195, v240
	s_waitcnt lgkmcnt(0)
	v_mfma_f32_32x32x16_bf16 v[0:15], v[216:219], v[232:235], v[0:15]
	v_mul_f32_e32 v200, 0x3dd53b94, v200
	v_exp_f32_e32 v200, v200
	s_cmp_eq_u64 vcc, exec
	s_cselect_b64 s[6:7], -1, 0
	v_mfma_f32_32x32x16_bf16 v[48:63], v[204:207], v[220:223], v[48:63]
	v_cndmask_b32_e64 v200, v200, 1.0, s[6:7]
	v_cmp_gt_f32_e32 vcc, 1.0, v200
	v_cndmask_b32_e64 v195, v240, v195, s[6:7]
	v_mul_f32_e32 v240, 0xbdd53b94, v195
	v_mov_b32_e32 v241, v240
	ds_read_b64_tr_b16 v[220:221], v190 offset:0x400
	ds_read_b64_tr_b16 v[222:223], v190 offset:0xc00
	v_mfma_f32_32x32x16_bf16 v[48:63], v[208:211], v[224:227], v[48:63]
	v_fmamk_f32 v112, v112, 0x3dd53b94, v240
	v_fmamk_f32 v113, v113, 0x3dd53b94, v240
	v_fmamk_f32 v114, v114, 0x3dd53b94, v240
	v_fmamk_f32 v115, v115, 0x3dd53b94, v240
	v_fmamk_f32 v116, v116, 0x3dd53b94, v240
	ds_read_b64_tr_b16 v[224:225], v190 offset:0x1400
	ds_read_b64_tr_b16 v[226:227], v190 offset:0x1c00
	v_mfma_f32_32x32x16_bf16 v[48:63], v[212:215], v[228:231], v[48:63]
	v_fmamk_f32 v117, v117, 0x3dd53b94, v240
	v_fmamk_f32 v118, v118, 0x3dd53b94, v240
	v_fmamk_f32 v119, v119, 0x3dd53b94, v240
	v_fmamk_f32 v120, v120, 0x3dd53b94, v240
	v_fmamk_f32 v121, v121, 0x3dd53b94, v240
	ds_read_b64_tr_b16 v[228:229], v190 offset:0x2400
	ds_read_b64_tr_b16 v[230:231], v190 offset:0x2c00
	ds_read_b64_tr_b16 v[232:233], v190 offset:0x3400
	ds_read_b64_tr_b16 v[234:235], v190 offset:0x3c00
	v_fmamk_f32 v122, v122, 0x3dd53b94, v240
	v_fmamk_f32 v123, v123, 0x3dd53b94, v240
	v_fmamk_f32 v124, v124, 0x3dd53b94, v240
	v_fmamk_f32 v125, v125, 0x3dd53b94, v240
	v_fmamk_f32 v126, v126, 0x3dd53b94, v240
	v_fmac_f32_e32 v241, 0x3dd53b94, v127
	v_exp_f32_e32 v112, v112
	s_waitcnt lgkmcnt(0)
	v_mfma_f32_32x32x16_bf16 v[48:63], v[216:219], v[236:239], v[48:63]
	v_exp_f32_e32 v113, v113
	v_exp_f32_e32 v114, v114
	v_mfma_f32_32x32x16_bf16 v[32:47], v[204:207], v[220:223], v[32:47]
	v_exp_f32_e32 v115, v115
	v_exp_f32_e32 v116, v116
	ds_read_b64_tr_b16 v[220:221], v190 offset:0x600
	ds_read_b64_tr_b16 v[222:223], v190 offset:0xe00
	v_mfma_f32_32x32x16_bf16 v[32:47], v[208:211], v[224:227], v[32:47]
	v_exp_f32_e32 v117, v117
	v_exp_f32_e32 v118, v118
	ds_read_b64_tr_b16 v[224:225], v190 offset:0x1600
	ds_read_b64_tr_b16 v[226:227], v190 offset:0x1e00
	v_mfma_f32_32x32x16_bf16 v[32:47], v[212:215], v[228:231], v[32:47]
	v_exp_f32_e32 v119, v119
	v_exp_f32_e32 v120, v120
	ds_read_b64_tr_b16 v[228:229], v190 offset:0x2600
	ds_read_b64_tr_b16 v[230:231], v190 offset:0x2e00
	ds_read_b64_tr_b16 v[236:237], v190 offset:0x3600
	ds_read_b64_tr_b16 v[238:239], v190 offset:0x3e00
	v_exp_f32_e32 v121, v121
	v_exp_f32_e32 v122, v122
	v_exp_f32_e32 v123, v123
	v_exp_f32_e32 v124, v124
	s_waitcnt lgkmcnt(0)
	v_mfma_f32_32x32x16_bf16 v[32:47], v[216:219], v[232:235], v[32:47]
	v_exp_f32_e32 v125, v125
	v_exp_f32_e32 v126, v126
	v_mfma_f32_32x32x16_bf16 v[16:31], v[204:207], v[220:223], v[16:31]
	v_exp_f32_e32 v127, v241
	v_pk_fma_f32 v[110:111], v[110:111], s[54:55], v[240:241] op_sel_hi:[1,0,0]
	v_mfma_f32_32x32x16_bf16 v[16:31], v[208:211], v[224:227], v[16:31]
	v_pk_fma_f32 v[108:109], v[108:109], s[54:55], v[240:241] op_sel_hi:[1,0,0]
	v_pk_fma_f32 v[106:107], v[106:107], s[54:55], v[240:241] op_sel_hi:[1,0,0]
	v_mfma_f32_32x32x16_bf16 v[16:31], v[212:215], v[228:231], v[16:31]
	v_pk_fma_f32 v[104:105], v[104:105], s[54:55], v[240:241] op_sel_hi:[1,0,0]
	v_pk_fma_f32 v[102:103], v[102:103], s[54:55], v[240:241] op_sel_hi:[1,0,0]
	v_mfma_f32_32x32x16_bf16 v[16:31], v[216:219], v[236:239], v[16:31]
	v_pk_fma_f32 v[100:101], v[100:101], s[54:55], v[240:241] op_sel_hi:[1,0,0]
	v_pk_fma_f32 v[98:99], v[98:99], s[54:55], v[240:241] op_sel_hi:[1,0,0]
	v_pk_fma_f32 v[96:97], v[96:97], s[54:55], v[240:241] op_sel_hi:[1,0,0]
	s_cbranch_vccz .Latt0_nrA
	s_nop 7
	s_nop 7
	s_and_saveexec_b64 s[38:39], s[4:5]
	ds_write_b32 v197, v200 offset:128
	s_or_b64 exec, exec, s[38:39]
	s_waitcnt lgkmcnt(0)
	v_add_u32_e32 v205, s77, v196
	ds_read_b128 v[206:209], v205 offset:224
	ds_read_b128 v[210:213], v205 offset:192
	ds_read_b128 v[214:217], v205 offset:160
	ds_read_b128 v[218:221], v205 offset:128
	s_waitcnt lgkmcnt(0)
	v_pk_mul_f32 v[12:13], v[12:13], v[206:207]
	v_pk_mul_f32 v[8:9], v[8:9], v[210:211]
	v_pk_mul_f32 v[4:5], v[4:5], v[214:215]
	v_pk_mul_f32 v[14:15], v[14:15], v[208:209]
	v_pk_mul_f32 v[10:11], v[10:11], v[212:213]
	v_pk_mul_f32 v[6:7], v[6:7], v[216:217]
	v_pk_mul_f32 v[2:3], v[2:3], v[220:221]
	v_pk_mul_f32 v[0:1], v[0:1], v[218:219]
	v_pk_mul_f32 v[60:61], v[60:61], v[206:207]
	v_pk_mul_f32 v[56:57], v[56:57], v[210:211]
	v_pk_mul_f32 v[52:53], v[52:53], v[214:215]
	v_pk_mul_f32 v[62:63], v[62:63], v[208:209]
	v_pk_mul_f32 v[58:59], v[58:59], v[212:213]
	v_pk_mul_f32 v[54:55], v[54:55], v[216:217]
	v_pk_mul_f32 v[50:51], v[50:51], v[220:221]
	v_pk_mul_f32 v[48:49], v[48:49], v[218:219]
	v_pk_mul_f32 v[44:45], v[44:45], v[206:207]
	v_pk_mul_f32 v[40:41], v[40:41], v[210:211]
	v_pk_mul_f32 v[36:37], v[36:37], v[214:215]
	v_pk_mul_f32 v[46:47], v[46:47], v[208:209]
	v_pk_mul_f32 v[42:43], v[42:43], v[212:213]
	v_pk_mul_f32 v[38:39], v[38:39], v[216:217]
	v_pk_mul_f32 v[34:35], v[34:35], v[220:221]
	v_pk_mul_f32 v[32:33], v[32:33], v[218:219]
	v_pk_mul_f32 v[28:29], v[28:29], v[206:207]
	v_pk_mul_f32 v[24:25], v[24:25], v[210:211]
	v_pk_mul_f32 v[20:21], v[20:21], v[214:215]
	v_pk_mul_f32 v[30:31], v[30:31], v[208:209]
	v_pk_mul_f32 v[26:27], v[26:27], v[212:213]
	v_pk_mul_f32 v[22:23], v[22:23], v[216:217]
	v_pk_mul_f32 v[18:19], v[18:19], v[220:221]
	v_pk_mul_f32 v[16:17], v[16:17], v[218:219]

.LBB0_520:
	s_min_u32 s6, s19, s42
	s_mul_i32 s6, s6, 0x30000
	v_add_f32_e32 v202, v202, v203
	s_add_u32 s6, s64, s6
	v_fmac_f32_e32 v202, v201, v198
	v_add_f32_e32 v198, v204, v205
	s_addc_u32 s7, s65, 0
	v_fmac_f32_e32 v198, v202, v200
	s_waitcnt vmcnt(0)
	v_lshl_add_u64 v[202:203], s[6:7], 0, v[152:153]
	s_waitcnt lgkmcnt(0)
	s_waitcnt vmcnt(0) lgkmcnt(0)
	s_barrier
	s_mov_b64 s[48:49], s[6:7]
	s_lshl_b64 s[6:7], s[36:37], 19
	s_add_u32 s6, s66, s6
	s_addc_u32 s7, s67, s7
	s_mov_b64 s[50:51], s[6:7]
	s_add_i32 s19, s19, 2
	s_cmp_ge_u32 s43, s33
	s_cbranch_scc1 .LBB0_522
	v_mov_b32_e32 v201, v206
	s_mov_b32 vcc_lo, 1
	s_branch .LBB0_503
